# role-aware sub-phase 1: workgroups expected to run a left-over MoE up unit skip their round-8 tile, the ones with only two down units convert it for them; hook split 2/1/1; loop-edge edit
# baseline (speedup 1.0000x reference)
; __device__ __forceinline__ void wg_conv_item(Frame& F, int l, int it) {
;     if (it < 208) { const int kt = it / 26, nt = it % 26;
;         wg_convert_tile(F, F.in[3] + (size_t)l * D * INW, INW, WSP(bf16_t, WS_WIN + l * SZ_WIN), D, 256 * kt, 256 * nt, -1, nullptr); return; }
;     it -= 208;
;     if (it < 320) { const int which = it / 64, rr = it % 64, kt = rr / 8, nt = rr % 8;
;         const int src = which == 0 ? 10 : 12 + which;
;         const size_t dst = which == 0 ? WS_WOUT : (which == 1 ? WS_WCQ : (which == 2 ? WS_WCK : (which == 3 ? WS_WCV : WS_WCO)));
;         wg_convert_tile(F, F.in[src] + (size_t)l * D * D, D, WSP(bf16_t, dst + l * SZ_SQ), D, 256 * kt, 256 * nt, -1, which == 1 ? F.in[11] + l * D : nullptr); return; }
;     it -= 320;
;     const int e = it / 48, rr = it % 48, kind = rr / 16, item = rr % 16;
.Lcv_special:
	s_bitcmp1_b32 s100, 26
	s_cbranch_scc1 .Lcv_sp2
	s_bitcmp1_b32 s100, 25
	s_cbranch_scc1 .Lcv_sp1
	s_mov_b32 s57, 0
	s_and_b32 s14, s9, 1
	s_lshl_b32 s14, s14, 3
	s_lshr_b32 s56, s9, 5
	s_add_i32 s14, s14, s56
	s_addk_i32 s14, 0x200
	s_branch .Lcv_dec
.Lcv_sp1:
	s_mov_b32 s57, 1
	s_lshr_b32 s14, s9, 5
	s_lshl_b32 s14, s14, 1
	s_and_b32 s56, s9, 1
	s_add_i32 s14, s14, s56
	s_addk_i32 s14, 0x800
	s_branch .Lcv_dec
.Lcv_sp2:
	s_mov_b32 s57, 1
	s_sub_u32 s14, s9, 24
	s_addk_i32 s14, 0x200

; __device__ __forceinline__ void wg_convert_layer(Frame& F, int l) {
;     __syncthreads();
;     for (int it = F.gw >> 3; it < WG_ITEMS_PER_LAYER; it += F.G) wg_conv_item(F, l, it);
; }
.Lcv_cnt:
	s_add_i32 s11, s11, -1
	s_cmp_lg_u32 s11, 0
	s_cbranch_scc1 .Lcv_item
	s_waitcnt vmcnt(0)
	s_barrier
	v_readlane_b32 s6, v253, 0
	v_readlane_b32 s7, v253, 1
	v_readlane_b32 s8, v253, 2
	v_readlane_b32 s9, v253, 3
	v_readlane_b32 s11, v253, 4
	v_readlane_b32 s12, v253, 5
	v_readlane_b32 s13, v253, 6
	v_readlane_b32 s14, v253, 7
	v_readlane_b32 s32, v253, 8
	v_readlane_b32 s38, v253, 9
	v_readlane_b32 s39, v253, 10
	v_readlane_b32 s55, v253, 11
	v_readlane_b32 s56, v253, 12
	v_readlane_b32 s57, v253, 13
	v_readlane_b32 s58, v253, 14
	v_readlane_b32 s59, v253, 15
	v_readlane_b32 s60, v253, 16
	v_readlane_b32 s61, v253, 17
	v_readlane_b32 s62, v253, 18
	v_readlane_b32 s63, v253, 19
	v_readlane_b32 s64, v253, 20
	v_readlane_b32 s65, v253, 21
	v_readlane_b32 s67, v253, 22
	v_readlane_b32 s70, v253, 23
	v_readlane_b32 s71, v253, 24
	v_readlane_b32 s76, v253, 25
	v_readlane_b32 s80, v253, 26
	v_readlane_b32 s81, v253, 27
	v_readlane_b32 s83, v253, 28
	v_readlane_b32 s95, v253, 29
	v_readlane_b32 s96, v253, 30
	v_readlane_b32 s97, v253, 31
	v_readlane_b32 s98, v253, 32
	v_readlane_b32 s99, v253, 33
	s_nop 7
	s_and_b32 s100, s100, 0xff
	s_cmp_eq_u32 s100, 0
	s_cbranch_scc1 .Lcv_ret_0
	s_cmp_eq_u32 s100, 1
	s_cbranch_scc1 .Lcv_ret_1
	s_cmp_eq_u32 s100, 2
	s_cbranch_scc1 .Lcv_ret_2
	s_cmp_eq_u32 s100, 3
	s_cbranch_scc1 .Lcv_ret_3
	s_cmp_eq_u32 s100, 4
	s_cbranch_scc1 .Lcv_ret_4
	s_cmp_eq_u32 s100, 5
	s_cbranch_scc1 .Lcv_ret_5
	s_cmp_eq_u32 s100, 6
	s_cbranch_scc1 .Lcv_ret_6
	s_cmp_eq_u32 s100, 7
	s_cbranch_scc1 .Lcv_ret_7
	s_cmp_eq_u32 s100, 8
	s_cbranch_scc1 .Lcv_ret_8
	s_cmp_eq_u32 s100, 9
	s_cbranch_scc1 .Lcv_ret_9
	s_cmp_eq_u32 s100, 10
	s_cbranch_scc1 .Lcv_ret_10
	s_cmp_eq_u32 s100, 11
	s_cbranch_scc1 .Lcv_ret_11
	s_cmp_eq_u32 s100, 12
	s_cbranch_scc1 .Lcv_ret_12
	s_cmp_eq_u32 s100, 13
	s_cbranch_scc1 .Lcv_ret_13
	s_branch .Lcv_ret_14

; __device__ __forceinline__ int moe_t1(int NT, int G) { const int t1 = NT < G / 4 ? NT : G / 4; return (4 * (NT - t1) < G / 2) ? t1 : NT; }
; #define INL(j) (((MK_PHMASK >> (j)) & 1) && INR(pb + (j)))
; __global__ void __launch_bounds__(NTHR, 2) mega_fwd(Args args) {
;     ...
; #pragma unroll 1
;         for (int sp = 0; sp < 3; ++sp) {
;             if (INL(10 + sp)) {
;                 if (sp == 0) moe_tables(F, l);
;                 const int NT = (int)F.MISC[MT_NT], T1 = moe_t1(NT, F.G), nUW = 4 * (NT - T1), nUR = (nUW + 7) & ~7;
;                 const bool doUp = sp == 0 || (sp == 1 && bx < nUW), doDown = (sp == 1 && bx >= nUR) || sp == 2;
;                 if (doUp) {
;                     SchedMoeUp Sc{F.MISC, (const char*)WSP(bf16_t, WS_W13 + l * SZ_W13), (char*)WSP(bf16_t, WS_HMID), WSP(int, WS_LIST), sp == 0 ? 0 : T1, sp == 0 ? 4 * T1 : nUW, bx, sp == 0 ? F.G : nUW};
;                     pg8::EpiSwiGLU E{WSP(float, WS_GATE), WSP(float, WS_RINV)};
;                     pg8::gemm_phase<pg8::EpiSwiGLU, SchedMoeUp, true, true>(F.wave, ring, D, D * 2, D * 2, (const char*)WSP(bf16_t, WS_XB), Sc, E);
;                 }
;                 if (doDown) {
;                     SchedMoeDown Sc{F.MISC, (const char*)WSP(bf16_t, WS_HMID), (const char*)WSP(bf16_t, WS_W2 + l * SZ_W2), (char*)WSP(bf16_t, WS_Y), sp == 1 ? 0 : T1, sp == 1 ? 8 * T1 : 8 * (NT - T1), sp == 1 ? bx - nUR : bx, sp == 1 ? F.G - nUR : F.G};
;                     pg8::EpiBf16 E{nullptr, 0};
;                     pg8::gemm_phase<pg8::EpiBf16, SchedMoeDown, false, false>(F.wave, ring, FH, FH * 2, FH * 2, nullptr, Sc, E);
;                 }
;             }
.LBB0_1552:
	v_readlane_b32 s100, v251, 3
	s_nop 3
	s_bitcmp1_b32 s100, 3
	s_cbranch_scc1 .Lcv_ret_9
	s_cmp_lg_u32 s87, 1
	s_cbranch_scc1 .Lcv_role_9
	s_cmp_lg_u32 s101, 8
	s_cbranch_scc1 .Lcv_role_9
	s_bfe_u32 s100, s100, 0x50003
	s_cmp_ge_u32 s100, 8
	s_cbranch_scc1 .Lcv_role2_9
	s_mov_b32 s101, 9
	s_branch .Lcv_ret_9
.Lcv_role2_9:
	s_cmp_lt_u32 s100, 24
	s_cbranch_scc1 .Lcv_role_9
	s_mov_b32 s100, 83886093
	s_branch .Lcv_run
.Lcv_ret_13:
.Lcv_role_9:
	s_add_i32 s100, s87, 8
	s_nop 0
	s_min_u32 s100, s100, 10
	s_cmp_ge_u32 s101, s100
	s_cbranch_scc1 .Lcv_ret_9
	s_lshl_b32 s100, s100, 8
	s_or_b32 s100, s100, 9
	s_branch .Lcv_run

; __device__ __forceinline__ int moe_t1(int NT, int G) { const int t1 = NT < G / 4 ? NT : G / 4; return (4 * (NT - t1) < G / 2) ? t1 : NT; }
; #define INL(j) (((MK_PHMASK >> (j)) & 1) && INR(pb + (j)))
; #define SEAM(k) do { if (INR(k) && INR((k) + 1)) xcd_barrier(bar); F.lane = lane_id_v(); F.tid = F.wave * 64 + F.lane; { int z_; asm volatile("s_mov_b32 %0, 0" : "=s"(z_)); F.ws = args.ws + z_; F.out = args.out + z_; F.ctl = (gu32*)(args.ws + WS_CTL) + z_; F.in = args.in + z_; F.gw = gw0 + z_; } } while (0)
; __global__ void __launch_bounds__(NTHR, 2) mega_fwd(Args args) {
;     ...
; #pragma unroll 1
;         for (int sp = 0; sp < 3; ++sp) {
;             if (INL(10 + sp)) {
;                 if (sp == 0) moe_tables(F, l);
;                 const int NT = (int)F.MISC[MT_NT], T1 = moe_t1(NT, F.G), nUW = 4 * (NT - T1), nUR = (nUW + 7) & ~7;
;                 const bool doUp = sp == 0 || (sp == 1 && bx < nUW), doDown = (sp == 1 && bx >= nUR) || sp == 2;
;                 if (doUp) {
;                     SchedMoeUp Sc{F.MISC, (const char*)WSP(bf16_t, WS_W13 + l * SZ_W13), (char*)WSP(bf16_t, WS_HMID), WSP(int, WS_LIST), sp == 0 ? 0 : T1, sp == 0 ? 4 * T1 : nUW, bx, sp == 0 ? F.G : nUW};
;                     pg8::EpiSwiGLU E{WSP(float, WS_GATE), WSP(float, WS_RINV)};
;                     pg8::gemm_phase<pg8::EpiSwiGLU, SchedMoeUp, true, true>(F.wave, ring, D, D * 2, D * 2, (const char*)WSP(bf16_t, WS_XB), Sc, E);
;                 }
;                 if (doDown) {
;                     SchedMoeDown Sc{F.MISC, (const char*)WSP(bf16_t, WS_HMID), (const char*)WSP(bf16_t, WS_W2 + l * SZ_W2), (char*)WSP(bf16_t, WS_Y), sp == 1 ? 0 : T1, sp == 1 ? 8 * T1 : 8 * (NT - T1), sp == 1 ? bx - nUR : bx, sp == 1 ? F.G - nUR : F.G};
;                     pg8::EpiBf16 E{nullptr, 0};
;                     pg8::gemm_phase<pg8::EpiBf16, SchedMoeDown, false, false>(F.wave, ring, FH, FH * 2, FH * 2, nullptr, Sc, E);
;                 }
;             }
;             SEAM(pb + 10 + sp);
;         }
.LBB0_1642:
	s_add_i32 s94, s94, 1
	s_cmp_lt_i32 s94, s75
	s_cselect_b64 s[4:5], -1, 0
	s_and_b64 s[4:5], s[70:71], s[4:5]
	s_andn2_b64 vcc, exec, s[4:5]
	s_cbranch_vccnz .LBB0_1551
	v_readlane_b32 s100, v251, 3
	s_nop 3
	s_bitcmp1_b32 s100, 3
	s_cbranch_scc0 .Lcv_ret_11
	s_cmp_lg_u32 s87, 1
	s_cbranch_scc1 .Lcv_role_11
	s_cmp_lg_u32 s101, 8
	s_cbranch_scc1 .Lcv_role_11
	s_bfe_u32 s100, s100, 0x50003
	s_cmp_ge_u32 s100, 8
	s_cbranch_scc1 .Lcv_role2_11
	s_mov_b32 s101, 9
	s_branch .Lcv_ret_11
.Lcv_role2_11:
	s_cmp_lt_u32 s100, 24
	s_cbranch_scc1 .Lcv_role_11
	s_mov_b32 s100, 83886094
	s_branch .Lcv_run
.Lcv_ret_14:
.Lcv_role_11:
	s_add_i32 s100, s87, 8
	s_nop 0
	s_min_u32 s100, s100, 10
	s_cmp_ge_u32 s101, s100
	s_cbranch_scc1 .Lcv_ret_11
	s_lshl_b32 s100, s100, 8
	s_or_b32 s100, s100, 11
	s_branch .Lcv_run
